# w_out GEMM: weight-tile rows permuted so each lane owns 8 contiguous bf16 outputs per row; X1 written with 16-byte stores (half the write requests), epilogue waits re-derived
# baseline (speedup 1.0000x reference)
;     ...
;     for (int i = 0; i < 2; ++i) { int R, C;
;         { const int b = tid * 16 + i * 8192; const int p = (b >> 7) & 15, fr_ = ((p & 1) << 3) | (p >> 1); R = (b >> 11) * 16 + fr_; C = ((((b >> 4) & 7) ^ (fr_ & 7))) * 16; }
;         const int Rb = Epi::PERM ? ((R & ~31) + perm32(R & 31)) : R;
;         voffA[i] = (unsigned)(R * KB + C); voffB[i] = (unsigned)(Rb * KB + C); }
;     constexpr bool GATHER = Sched::GATHER;
;     unsigned vG[2][2];
;     auto load_rows = [&](int buf, int nvalid) { const int t_ = (wid << 6) | lane_id();
; #pragma unroll
;         for (int i = 0; i < 2; ++i) { const int b = t_ * 16 + i * 8192; const int p = (b >> 7) & 15, fr_ = ((p & 1) << 3) | (p >> 1); const int R = (b >> 11) * 16 + fr_, C = ((((b >> 4) & 7) ^ (fr_ & 7))) * 16;
; #pragma unroll
;             for (int hh_ = 0; hh_ < 2; ++hh_) { const int rr = hh_ * 128 + R; const unsigned slot = ((const LAS unsigned*)(lds + LDS_CTL_OFF + 2048))[buf * 256 + rr];
;                 vG[hh_][i] = (rr < nvalid ? (slot >> 2) * (unsigned)KB : 0u) + (unsigned)C; } } };
;     constexpr bool ETAB = Sched::ETAB;
;     auto dma_etab = [&](const Unit& u_, int buf) {
;         if constexpr (ETAB) { if ((wid & ~1) == 4) __builtin_amdgcn_raw_ptr_buffer_load_lds(rsrc, (LAS void*)(lds + LDS_CTL_OFF + 2048 + (wid - 4) * 2048 + buf * 1024), 16, lane_id() * 16, (int)S.etab_off(u_, wid - 4), 0, 0); } };
;     constexpr bool BIAS = Sched::BIAS;
;     auto dma_bias = [&](const Unit& u_, int buf) {
;         if constexpr (BIAS) { if ((wid == 6 || wid == 7) && lane_id() < 32) __builtin_amdgcn_raw_ptr_buffer_load_lds(rsrc, (LAS void*)(lds + LDS_CTL_OFF + 4096 + buf * 1024 + (wid - 6) * 512), 16, lane_id() * 16, (int)S.bias_off(u_, wid - 6), 0, 0); } };
;     auto dma_list = [&](unsigned goff, int buf) {
;         if (wid == 4) __builtin_amdgcn_raw_ptr_buffer_load_lds(rsrc, (LAS void*)(lds + LDS_CTL_OFF + 2048 + buf * 1024), 16, lane_id() * 16, (int)goff, 0, 0); };
;     const unsigned kstep = 128u;
;     const unsigned hstep = (unsigned)(HALF * KB);
;     const unsigned ldsw = (unsigned)wid * 1024u;
;     int aoff[2], boff[2];
; #pragma unroll
;     for (int x = 0; x < 2; ++x) { const int ch = F8 ? (2 * fq + x) : (fq + 4 * x); const int o = ((((fr & 7) << 1) | (fr >> 3)) << 7) + ((ch ^ (fr & 7)) << 4); aoff[x] = wr * 8192 + o; boff[x] = wc * 4096 + o; }
;     ...
;     if constexpr (SP2) {
.LBB0_947:
	s_add_i32 s0, s0, s1
	s_ashr_i32 s1, s0, 31
	s_lshr_b32 s1, s1, 26
	s_add_i32 s1, s0, s1
	s_ashr_i32 s3, s1, 6
	s_and_b32 s1, s1, 0xffc0
	s_sub_i32 s0, s0, s1
	v_lshrrev_b32_e32 v1, 4, v2
	s_bfe_i32 s1, s0, 0x80000
	v_xor_b32_e32 v5, v1, v0
	v_lshrrev_b32_e32 v6, 3, v2
	s_bfe_u32 s1, s1, 0x3000c
	v_bfe_u32 v3, v2, 4, 3
	v_and_b32_e32 v4, 8, v0
	v_lshlrev_b32_e32 v5, 4, v5
	v_and_b32_e32 v6, 0x1ffff0, v6
	s_add_i32 s1, s0, s1
	v_and_b32_e32 v5, 0x70, v5
	v_or3_b32 v6, v4, v6, v3
	s_bfe_i32 s11, s1, 0x80000
	s_and_b32 s1, s1, 0xf8
	s_waitcnt vmcnt(14)
	v_lshl_or_b32 v136, v6, 11, v5
	v_mov_b32_e32 v6, 0x2000
	s_ashr_i32 s2, s18, 6
	s_sub_i32 s0, s0, s1
	v_lshl_add_u32 v2, v2, 4, v6
	s_lshl_b32 s10, s2, 10
	s_lshl_b32 s3, s3, 3
	s_sext_i32_i16 s11, s11
	s_sext_i32_i8 s0, s0
	v_lshrrev_b32_e32 v2, 7, v2
	v_readlane_b32 s12, v254, 2
	s_add_i32 s67, s3, s0
	s_ashr_i32 s68, s11, 3
	s_add_i32 s0, s10, 0
	v_and_b32_e32 v2, 0x1ffff0, v2
	v_readlane_b32 s14, v254, 4
	v_readlane_b32 s15, v254, 5
	s_lshl_b32 s3, s68, 19
	s_add_i32 s1, s0, 0x10000
	v_or3_b32 v2, v4, v2, v3
	s_mov_b32 s7, 0x20000
	s_mov_b32 s6, -1
	s_and_b32 s5, s15, 0xffff
	s_mov_b32 s4, s14
	s_add_i32 s69, s3, 0x1b00000
	s_mov_b32 m0, s1
	s_add_i32 s33, s0, 0x12000
	v_lshl_or_b32 v137, v2, 11, v5
	v_lshrrev_b32_e32 v252, 11, v136
	v_and_b32_e32 v253, 12, v252
	v_lshlrev_b32_e32 v253, 1, v253
	v_bfe_u32 v210, v252, 4, 1
	v_lshl_or_b32 v253, v210, 2, v253
	v_and_b32_e32 v252, 0xffffffe3, v252
	v_or_b32_e32 v252, v252, v253
	v_and_b32_e32 v253, 0x7ff, v136
	v_lshl_or_b32 v210, v252, 11, v253
	v_lshrrev_b32_e32 v252, 11, v137
	v_and_b32_e32 v253, 12, v252
	v_lshlrev_b32_e32 v253, 1, v253
	v_bfe_u32 v211, v252, 4, 1
	v_lshl_or_b32 v253, v211, 2, v253
	v_and_b32_e32 v252, 0xffffffe3, v252
	v_or_b32_e32 v252, v252, v253
	v_and_b32_e32 v253, 0x7ff, v137
	v_lshl_or_b32 v211, v252, 11, v253
	buffer_load_dwordx4 v210, s[4:7], s69 offen lds
	s_mov_b32 m0, s33
	s_add_i32 s34, s0, 0x14000
	buffer_load_dwordx4 v211, s[4:7], s69 offen lds
	s_add_i32 s10, s3, 0x1b40000
	s_mov_b32 m0, s34
	s_add_i32 s35, s0, 0x16000
	s_lshl_b32 s19, s67, 19
	buffer_load_dwordx4 v210, s[4:7], s10 offen lds
	s_mov_b32 m0, s35
	s_add_i32 s70, s19, 0x46e00000
	buffer_load_dwordx4 v211, s[4:7], s10 offen lds
	s_mov_b32 m0, s0
	s_add_i32 s48, s0, 0x2000
	buffer_load_dwordx4 v136, s[4:7], s70 offen lds
	s_mov_b32 m0, s48
	s_add_i32 s49, s0, 0x4000
	buffer_load_dwordx4 v137, s[4:7], s70 offen lds
	s_add_i32 s10, s19, 0x46e40000
	s_mov_b32 m0, s49
	s_add_i32 s50, s0, 0x6000
	buffer_load_dwordx4 v136, s[4:7], s10 offen lds
	s_mov_b32 m0, s50
	s_ashr_i32 s20, s18, 8
	buffer_load_dwordx4 v137, s[4:7], s10 offen lds
	s_cmp_eq_u32 s20, 1
	s_cselect_b64 s[10:11], -1, 0
	s_cmp_lg_u32 s20, 1
	s_mov_b32 s51, 0
	v_readlane_b32 s13, v254, 3
	s_cbranch_scc1 .LBB0_949
	s_barrier
.LBB0_949:
	v_readlane_b32 s40, v254, 2
	v_readlane_b32 s42, v254, 4
	v_readlane_b32 s43, v254, 5
	s_add_u32 s12, s42, 0x74e00000
	s_addc_u32 s13, s43, 0
	s_add_u32 s14, s42, 0x22980000
	s_addc_u32 s15, s43, 0
	s_add_u32 s16, s42, 0x22948000
	s_addc_u32 s17, s43, 0
	s_add_i32 s52, s0, 0x18000
	s_add_i32 s21, s3, 0x1b00080
	s_mov_b32 m0, s52
	s_add_i32 s53, s0, 0x1a000
	s_waitcnt vmcnt(2)
	s_barrier
	buffer_load_dwordx4 v210, s[4:7], s21 offen lds
	s_mov_b32 m0, s53
	s_add_i32 s54, s0, 0x8000
	buffer_load_dwordx4 v211, s[4:7], s21 offen lds
	s_add_i32 s19, s19, 0x46e00080
	s_mov_b32 m0, s54
	s_add_i32 s55, s0, 0xa000
	buffer_load_dwordx4 v136, s[4:7], s19 offen lds
	s_mov_b32 m0, s55
	s_add_i32 s56, s0, 0x1c000
	buffer_load_dwordx4 v137, s[4:7], s19 offen lds
	s_add_i32 s3, s3, 0x1b40080
	s_mov_b32 m0, s56
	s_add_i32 s57, s0, 0x1e000
	buffer_load_dwordx4 v210, s[4:7], s3 offen lds
	s_mov_b32 m0, s57
	v_and_b32_e32 v3, 7, v0
	buffer_load_dwordx4 v211, s[4:7], s3 offen lds
	v_lshlrev_b32_e32 v0, 4, v0
	v_and_b32_e32 v0, 0x80, v0
	s_and_b32 s2, s2, 3
	v_and_b32_e32 v2, 3, v1
	v_lshl_or_b32 v0, v3, 8, v0
	v_bitop3_b32 v1, v1, v3, 3 bitop3:0x6c
	s_lshl_b32 s3, s20, 13
	s_lshl_b32 s4, s2, 12
	v_lshl_or_b32 v1, v1, 4, v0
	v_or_b32_e32 v4, s3, v1
	v_or_b32_e32 v138, s4, v1
	v_bitop3_b32 v1, v2, v3, 4 bitop3:0x36
	s_add_i32 s58, s0, 0xc000
	v_lshl_or_b32 v0, v1, 4, v0
	s_cmpk_lt_u32 s18, 0x100
	v_or_b32_e32 v139, s4, v0
	s_cselect_b64 s[18:19], -1, 0
	s_lshl_b32 s60, s2, 5
	s_add_i32 s2, 0, 0x10000
	s_waitcnt vmcnt(27)
	v_add_u32_e32 v140, s2, v138
	v_add_u32_e32 v141, s2, v139
	s_add_i32 s2, 0, 0x10800
	v_add_u32_e32 v142, s2, v138
	v_add_u32_e32 v143, s2, v139
	s_add_i32 s2, 0, 0x14000
	s_waitcnt vmcnt(26)
	v_add_u32_e32 v144, s2, v138
	v_add_u32_e32 v145, s2, v139
	s_add_i32 s2, 0, 0x14800
	s_waitcnt vmcnt(6)
	v_add_u32_e32 v146, s2, v138
	v_add_u32_e32 v147, s2, v139
	s_add_i32 s2, 0, 0x18800
	v_readlane_b32 s41, v254, 3
	v_or_b32_e32 v1, s3, v0
	s_waitcnt vmcnt(25)
	v_add_u32_e32 v150, s2, v138
	v_add_u32_e32 v151, s2, v139
	s_add_i32 s2, 0, 0x1c800
	s_lshl_b32 s59, s20, 6
	s_add_i32 s61, s0, 0xe000
	v_add_u32_e32 v148, 0, v4
	v_add_u32_e32 v149, 0, v1
	s_waitcnt vmcnt(14)
	v_add_u32_e32 v152, s2, v138
	v_add_u32_e32 v153, s2, v139
	s_mov_b64 s[20:21], 0x1c4000
	s_mov_b32 s62, 0x1c4000
	s_mov_b64 s[22:23], 0x40000
	s_mov_b64 s[38:39], 0x48000
	s_mov_b64 s[40:41], 0x50000
	s_mov_b64 s[42:43], 0x58000
	s_mov_b32 s65, s70
	s_mov_b32 s66, s69
	s_barrier
	s_branch .LBB0_952

; #define PG8_STAGE(bufoff, gbase, voff) do { _Pragma("unroll") for (int _i = 0; _i < 2; ++_i) \
;         __builtin_amdgcn_raw_ptr_buffer_load_lds(rsrc, (LAS void*)(lds + (bufoff) + ldsw + _i * 8192), 16, (int)(voff)[_i], (int)(gbase), 0, 0); } while (0)
; #define PG8_STAGE_A(bufoff, h, goff) do { if constexpr (GATHER) { PG8_STAGE(bufoff, goff, vG[h]); } else { PG8_STAGE(bufoff, (goff) + (h) * hstep, voffA); } } while (0)
; #define PG8_WAIT_V(n) asm volatile("s_waitcnt vmcnt(" #n ")" ::: "memory")
; #define PG8_WAIT_L(n) asm volatile("s_waitcnt lgkmcnt(" #n ")" ::: "memory")
; #define PG8_BAR __builtin_amdgcn_s_barrier()
; #define PG8_SCHED __builtin_amdgcn_sched_barrier(0)
;     DI int row_cnt(const pg8::Unit& u) const { return __builtin_amdgcn_readfirstlane(tab[u.a0]) - u.ldc; }
;     ...
;         for (int t = 0; t < nt; t += 2) {
;             const bool last = (t == nt - 2);
;             const unsigned a1 = cA + (unsigned)(t + 1) * kstep;
;             const unsigned a2 = last ? nA : cA + (unsigned)(t + 2) * kstep, b2 = last ? nB : cB + (unsigned)(t + 2) * kstep;
;             const unsigned a3 = a2 + kstep, b3 = b2 + kstep;
;             if constexpr (SP2) {
;             PG8_LDB(B0, 0, 0); PG8_LDB(B1, 0, 1); PG8_SCHED; PG8_LDA(At, 0, 0); PG8_STAGE_A(PG8_SA(1, 1), 1, a1);
;             if constexpr (GATHER) { if (last && has_next) load_rows((ui + 1) & 1, S.row_cnt(nxt)); }
;             PG8_WAIT_V(8); PG8_WAIT_L(0); PG8_BAR; PG8_MMA(0, 0, At, B0); PG8_MMA(0, 1, At, B1); PG8_BAR; PG8_SCHED;
;             PG8_LDA(At, 0, 1); PG8_STAGE(PG8_SB(0, 0), b2, voffB); PG8_STAGE(PG8_SB(0, 1), b2 + hstep, voffB); PG8_STAGE_A(PG8_SA(0, 0), 0, a2);
;             PG8_WAIT_V(8); PG8_WAIT_L(0); PG8_BAR; PG8_MMA(1, 0, At, B0); PG8_MMA(1, 1, At, B1); PG8_BAR; PG8_SCHED;
.LBB0_959:
	ds_read_b128 v[128:131], v140
	ds_read_b128 v[132:135], v141
	ds_read_b128 v[154:157], v142
	ds_read_b128 v[158:161], v143
	ds_read_b128 v[162:165], v144
	ds_read_b128 v[166:169], v145
	ds_read_b128 v[170:173], v146
	ds_read_b128 v[174:177], v147
	s_add_i32 s4, s2, 0xfffc0080
	s_cmp_eq_u32 s69, 12
	s_cselect_b32 s72, s65, s4
	s_cselect_b32 s71, s66, s3
	s_add_i32 s70, s72, 0x80
	s_mov_b32 s4, s74
	s_mov_b32 m0, s58
	ds_read_b128 v[178:181], v148
	ds_read_b128 v[182:185], v148 offset:2048
	ds_read_b128 v[186:189], v149
	ds_read_b128 v[190:193], v149 offset:2048
	ds_read_b128 v[194:197], v148 offset:4096
	ds_read_b128 v[198:201], v148 offset:6144
	ds_read_b128 v[202:205], v149 offset:4096
	ds_read_b128 v[206:209], v149 offset:6144
	buffer_load_dwordx4 v136, s[4:7], s2 offen lds
	s_mov_b32 m0, s61
	s_nop 0
	buffer_load_dwordx4 v137, s[4:7], s2 offen lds
	s_waitcnt vmcnt(8)
	s_waitcnt lgkmcnt(0)
	s_barrier
	s_setprio 1
	s_waitcnt lgkmcnt(7)
	v_mfma_i32_16x16x64_i8 v[124:127], v[128:131], v[178:181], v[124:127]
	v_mfma_i32_16x16x64_i8 v[120:123], v[154:157], v[178:181], v[120:123]
	s_waitcnt lgkmcnt(6)
	v_mfma_i32_16x16x64_i8 v[108:111], v[128:131], v[182:185], v[108:111]
	v_mfma_i32_16x16x64_i8 v[104:107], v[154:157], v[182:185], v[104:107]
	s_waitcnt lgkmcnt(3)
	v_mfma_i32_16x16x64_i8 v[92:95], v[128:131], v[194:197], v[92:95]
	v_mfma_i32_16x16x64_i8 v[88:91], v[154:157], v[194:197], v[88:91]
	s_waitcnt lgkmcnt(2)
	v_mfma_i32_16x16x64_i8 v[76:79], v[128:131], v[198:201], v[76:79]
	v_mfma_i32_16x16x64_i8 v[72:75], v[154:157], v[198:201], v[72:75]
	v_mfma_i32_16x16x64_i8 v[124:127], v[132:135], v[186:189], v[124:127]
	v_mfma_i32_16x16x64_i8 v[120:123], v[158:161], v[186:189], v[120:123]
	v_mfma_i32_16x16x64_i8 v[108:111], v[132:135], v[190:193], v[108:111]
	v_mfma_i32_16x16x64_i8 v[104:107], v[158:161], v[190:193], v[104:107]
	s_waitcnt lgkmcnt(1)
	v_mfma_i32_16x16x64_i8 v[92:95], v[132:135], v[202:205], v[92:95]
	v_mfma_i32_16x16x64_i8 v[88:91], v[158:161], v[202:205], v[88:91]
	s_waitcnt lgkmcnt(0)
	v_mfma_i32_16x16x64_i8 v[76:79], v[132:135], v[206:209], v[76:79]
	v_mfma_i32_16x16x64_i8 v[72:75], v[158:161], v[206:209], v[72:75]
	s_setprio 0
	s_setprio 1
	v_mfma_i32_16x16x64_i8 v[116:119], v[162:165], v[178:181], v[116:119]
	v_mfma_i32_16x16x64_i8 v[112:115], v[170:173], v[178:181], v[112:115]
	v_mfma_i32_16x16x64_i8 v[100:103], v[162:165], v[182:185], v[100:103]
	v_mfma_i32_16x16x64_i8 v[96:99], v[170:173], v[182:185], v[96:99]
	v_mfma_i32_16x16x64_i8 v[84:87], v[162:165], v[194:197], v[84:87]
	v_mfma_i32_16x16x64_i8 v[80:83], v[170:173], v[194:197], v[80:83]
	v_mfma_i32_16x16x64_i8 v[68:71], v[162:165], v[198:201], v[68:71]
	v_mfma_i32_16x16x64_i8 v[64:67], v[170:173], v[198:201], v[64:67]
	v_mfma_i32_16x16x64_i8 v[116:119], v[166:169], v[186:189], v[116:119]
	v_mfma_i32_16x16x64_i8 v[112:115], v[174:177], v[186:189], v[112:115]
	v_mfma_i32_16x16x64_i8 v[100:103], v[166:169], v[190:193], v[100:103]
	v_mfma_i32_16x16x64_i8 v[96:99], v[174:177], v[190:193], v[96:99]
	v_mfma_i32_16x16x64_i8 v[84:87], v[166:169], v[202:205], v[84:87]
	v_mfma_i32_16x16x64_i8 v[80:83], v[174:177], v[202:205], v[80:83]
	v_mfma_i32_16x16x64_i8 v[68:71], v[166:169], v[206:209], v[68:71]
	v_mfma_i32_16x16x64_i8 v[64:67], v[174:177], v[206:209], v[64:67]
	s_setprio 0
	s_barrier
	s_mov_b32 m0, s1
	ds_read_b128 v[178:181], v148 offset:16384
	ds_read_b128 v[182:185], v148 offset:18432
	ds_read_b128 v[186:189], v149 offset:16384
	ds_read_b128 v[190:193], v149 offset:18432
	ds_read_b128 v[194:197], v148 offset:20480
	ds_read_b128 v[198:201], v148 offset:22528
	ds_read_b128 v[202:205], v149 offset:20480
	ds_read_b128 v[206:209], v149 offset:22528
	buffer_load_dwordx4 v210, s[4:7], s71 offen lds
	s_mov_b32 m0, s33
	s_add_i32 s73, s71, 0x40000
	buffer_load_dwordx4 v211, s[4:7], s71 offen lds
	s_mov_b32 m0, s34
	s_nop 0
	buffer_load_dwordx4 v210, s[4:7], s73 offen lds
	s_mov_b32 m0, s35
	s_nop 0
	buffer_load_dwordx4 v211, s[4:7], s73 offen lds
	s_mov_b32 m0, s0
	s_nop 0
	buffer_load_dwordx4 v136, s[4:7], s72 offen lds
	s_mov_b32 m0, s48
	s_nop 0
	buffer_load_dwordx4 v137, s[4:7], s72 offen lds
	s_waitcnt vmcnt(8)
	s_waitcnt lgkmcnt(0)
	s_barrier
	s_setprio 1
	s_waitcnt lgkmcnt(7)
	v_mfma_i32_16x16x64_i8 v[60:63], v[128:131], v[178:181], v[60:63]
	v_mfma_i32_16x16x64_i8 v[56:59], v[154:157], v[178:181], v[56:59]
	s_waitcnt lgkmcnt(6)
	v_mfma_i32_16x16x64_i8 v[44:47], v[128:131], v[182:185], v[44:47]
	v_mfma_i32_16x16x64_i8 v[40:43], v[154:157], v[182:185], v[40:43]
	s_waitcnt lgkmcnt(3)
	v_mfma_i32_16x16x64_i8 v[28:31], v[128:131], v[194:197], v[28:31]
	v_mfma_i32_16x16x64_i8 v[24:27], v[154:157], v[194:197], v[24:27]
	s_waitcnt lgkmcnt(2)
	v_mfma_i32_16x16x64_i8 v[12:15], v[128:131], v[198:201], v[12:15]
	v_mfma_i32_16x16x64_i8 v[8:11], v[154:157], v[198:201], v[8:11]
	v_mfma_i32_16x16x64_i8 v[60:63], v[132:135], v[186:189], v[60:63]
	v_mfma_i32_16x16x64_i8 v[56:59], v[158:161], v[186:189], v[56:59]
	v_mfma_i32_16x16x64_i8 v[44:47], v[132:135], v[190:193], v[44:47]
	v_mfma_i32_16x16x64_i8 v[40:43], v[158:161], v[190:193], v[40:43]
	s_waitcnt lgkmcnt(1)
	v_mfma_i32_16x16x64_i8 v[28:31], v[132:135], v[202:205], v[28:31]
	v_mfma_i32_16x16x64_i8 v[24:27], v[158:161], v[202:205], v[24:27]
	s_waitcnt lgkmcnt(0)
	v_mfma_i32_16x16x64_i8 v[12:15], v[132:135], v[206:209], v[12:15]
	v_mfma_i32_16x16x64_i8 v[8:11], v[158:161], v[206:209], v[8:11]
	s_setprio 0
	s_setprio 1
	v_mfma_i32_16x16x64_i8 v[52:55], v[162:165], v[178:181], v[52:55]
	v_mfma_i32_16x16x64_i8 v[48:51], v[170:173], v[178:181], v[48:51]
	v_mfma_i32_16x16x64_i8 v[36:39], v[162:165], v[182:185], v[36:39]
	v_mfma_i32_16x16x64_i8 v[32:35], v[170:173], v[182:185], v[32:35]
	v_mfma_i32_16x16x64_i8 v[20:23], v[162:165], v[194:197], v[20:23]
	v_mfma_i32_16x16x64_i8 v[16:19], v[170:173], v[194:197], v[16:19]
	v_mfma_i32_16x16x64_i8 v[4:7], v[162:165], v[198:201], v[4:7]
	v_mfma_i32_16x16x64_i8 v[0:3], v[170:173], v[198:201], v[0:3]
	v_mfma_i32_16x16x64_i8 v[52:55], v[166:169], v[186:189], v[52:55]
	v_mfma_i32_16x16x64_i8 v[48:51], v[174:177], v[186:189], v[48:51]
	v_mfma_i32_16x16x64_i8 v[36:39], v[166:169], v[190:193], v[36:39]
	v_mfma_i32_16x16x64_i8 v[32:35], v[174:177], v[190:193], v[32:35]
	v_mfma_i32_16x16x64_i8 v[20:23], v[166:169], v[202:205], v[20:23]
	v_mfma_i32_16x16x64_i8 v[16:19], v[174:177], v[202:205], v[16:19]
	v_mfma_i32_16x16x64_i8 v[4:7], v[166:169], v[206:209], v[4:7]
	v_mfma_i32_16x16x64_i8 v[0:3], v[174:177], v[206:209], v[0:3]
	s_setprio 0
	s_barrier
; #define PG8_STAGE(bufoff, gbase, voff) do { _Pragma("unroll") for (int _i = 0; _i < 2; ++_i) \
;         __builtin_amdgcn_raw_ptr_buffer_load_lds(rsrc, (LAS void*)(lds + (bufoff) + ldsw + _i * 8192), 16, (int)(voff)[_i], (int)(gbase), 0, 0); } while (0)
; #define PG8_STAGE_A(bufoff, h, goff) do { if constexpr (GATHER) { PG8_STAGE(bufoff, goff, vG[h]); } else { PG8_STAGE(bufoff, (goff) + (h) * hstep, voffA); } } while (0)
; #define PG8_WAIT_V(n) asm volatile("s_waitcnt vmcnt(" #n ")" ::: "memory")
; #define PG8_WAIT_L(n) asm volatile("s_waitcnt lgkmcnt(" #n ")" ::: "memory")
; #define PG8_BAR __builtin_amdgcn_s_barrier()
; #define PG8_SCHED __builtin_amdgcn_sched_barrier(0)
;     ...
;             PG8_LDB(B0, 1, 0); PG8_LDB(B1, 1, 1); PG8_SCHED; PG8_LDA(At, 1, 0); PG8_STAGE_A(PG8_SA(0, 1), 1, a2);
;             PG8_WAIT_V(8); PG8_WAIT_L(0); PG8_BAR; PG8_MMA(0, 0, At, B0); PG8_MMA(0, 1, At, B1); PG8_BAR; PG8_SCHED;
;             PG8_LDA(At, 1, 1); PG8_STAGE(PG8_SB(1, 0), b3, voffB); PG8_STAGE(PG8_SB(1, 1), b3 + hstep, voffB); PG8_STAGE_A(PG8_SA(1, 0), 0, a3);
;             PG8_WAIT_V(8); PG8_WAIT_L(0); PG8_BAR; PG8_MMA(1, 0, At, B0); PG8_MMA(1, 1, At, B1); PG8_BAR; PG8_SCHED;
;     ...
;         if constexpr (ALIGN_EPI) { if (wr == 0) PG8_BAR; }
	s_add_i32 s73, 0, 0x18000
	v_add_u32_e32 v128, s73, v138
	v_add_u32_e32 v132, s73, v139
	s_add_i32 s73, 0, 0x1c000
	v_add_u32_e32 v162, s73, v138
	v_add_u32_e32 v166, s73, v139
	ds_read_b128 v[128:131], v128
	ds_read_b128 v[132:135], v132
	ds_read_b128 v[154:157], v150
	ds_read_b128 v[158:161], v151
	ds_read_b128 v[162:165], v162
	ds_read_b128 v[166:169], v166
	ds_read_b128 v[170:173], v152
	ds_read_b128 v[174:177], v153
	s_add_i32 s72, s72, 0x40000
	s_mov_b32 m0, s49
	ds_read_b128 v[178:181], v148 offset:32768
	ds_read_b128 v[182:185], v148 offset:34816
	ds_read_b128 v[186:189], v149 offset:32768
	ds_read_b128 v[190:193], v149 offset:34816
	ds_read_b128 v[194:197], v148 offset:36864
	ds_read_b128 v[198:201], v148 offset:38912
	ds_read_b128 v[202:205], v149 offset:36864
	ds_read_b128 v[206:209], v149 offset:38912
	buffer_load_dwordx4 v136, s[4:7], s72 offen lds
	s_mov_b32 m0, s50
	s_nop 0
	buffer_load_dwordx4 v137, s[4:7], s72 offen lds
	s_waitcnt vmcnt(8)
	s_waitcnt lgkmcnt(0)
	s_barrier
	s_setprio 1
	s_waitcnt lgkmcnt(7)
	v_mfma_i32_16x16x64_i8 v[124:127], v[128:131], v[178:181], v[124:127]
	v_mfma_i32_16x16x64_i8 v[120:123], v[154:157], v[178:181], v[120:123]
	s_waitcnt lgkmcnt(6)
	v_mfma_i32_16x16x64_i8 v[108:111], v[128:131], v[182:185], v[108:111]
	v_mfma_i32_16x16x64_i8 v[104:107], v[154:157], v[182:185], v[104:107]
	s_waitcnt lgkmcnt(3)
	v_mfma_i32_16x16x64_i8 v[92:95], v[128:131], v[194:197], v[92:95]
	v_mfma_i32_16x16x64_i8 v[88:91], v[154:157], v[194:197], v[88:91]
	s_waitcnt lgkmcnt(2)
	v_mfma_i32_16x16x64_i8 v[76:79], v[128:131], v[198:201], v[76:79]
	v_mfma_i32_16x16x64_i8 v[72:75], v[154:157], v[198:201], v[72:75]
	v_mfma_i32_16x16x64_i8 v[124:127], v[132:135], v[186:189], v[124:127]
	v_mfma_i32_16x16x64_i8 v[120:123], v[158:161], v[186:189], v[120:123]
	v_mfma_i32_16x16x64_i8 v[108:111], v[132:135], v[190:193], v[108:111]
	v_mfma_i32_16x16x64_i8 v[104:107], v[158:161], v[190:193], v[104:107]
	s_waitcnt lgkmcnt(1)
	v_mfma_i32_16x16x64_i8 v[92:95], v[132:135], v[202:205], v[92:95]
	v_mfma_i32_16x16x64_i8 v[88:91], v[158:161], v[202:205], v[88:91]
	s_waitcnt lgkmcnt(0)
	v_mfma_i32_16x16x64_i8 v[76:79], v[132:135], v[206:209], v[76:79]
	v_mfma_i32_16x16x64_i8 v[72:75], v[158:161], v[206:209], v[72:75]
	s_setprio 0
	s_setprio 1
	v_mfma_i32_16x16x64_i8 v[116:119], v[162:165], v[178:181], v[116:119]
	v_mfma_i32_16x16x64_i8 v[112:115], v[170:173], v[178:181], v[112:115]
	v_mfma_i32_16x16x64_i8 v[100:103], v[162:165], v[182:185], v[100:103]
	v_mfma_i32_16x16x64_i8 v[96:99], v[170:173], v[182:185], v[96:99]
	v_mfma_i32_16x16x64_i8 v[84:87], v[162:165], v[194:197], v[84:87]
	v_mfma_i32_16x16x64_i8 v[80:83], v[170:173], v[194:197], v[80:83]
	v_mfma_i32_16x16x64_i8 v[68:71], v[162:165], v[198:201], v[68:71]
	v_mfma_i32_16x16x64_i8 v[64:67], v[170:173], v[198:201], v[64:67]
	v_mfma_i32_16x16x64_i8 v[116:119], v[166:169], v[186:189], v[116:119]
	v_mfma_i32_16x16x64_i8 v[112:115], v[174:177], v[186:189], v[112:115]
	v_mfma_i32_16x16x64_i8 v[100:103], v[166:169], v[190:193], v[100:103]
	v_mfma_i32_16x16x64_i8 v[96:99], v[174:177], v[190:193], v[96:99]
	v_mfma_i32_16x16x64_i8 v[84:87], v[166:169], v[202:205], v[84:87]
	v_mfma_i32_16x16x64_i8 v[80:83], v[174:177], v[202:205], v[80:83]
	v_mfma_i32_16x16x64_i8 v[68:71], v[166:169], v[206:209], v[68:71]
	v_mfma_i32_16x16x64_i8 v[64:67], v[174:177], v[206:209], v[64:67]
	s_setprio 0
	s_barrier
	s_mov_b32 m0, s52
	s_add_i32 s72, s71, 0x80
	ds_read_b128 v[178:181], v148 offset:49152
	ds_read_b128 v[182:185], v148 offset:51200
	ds_read_b128 v[186:189], v149 offset:49152
	ds_read_b128 v[190:193], v149 offset:51200
	ds_read_b128 v[194:197], v148 offset:53248
	ds_read_b128 v[198:201], v148 offset:55296
	ds_read_b128 v[202:205], v149 offset:53248
	ds_read_b128 v[206:209], v149 offset:55296
	buffer_load_dwordx4 v210, s[4:7], s72 offen lds
	s_mov_b32 m0, s53
	s_add_i32 s71, s71, 0x40080
	buffer_load_dwordx4 v211, s[4:7], s72 offen lds
	s_mov_b32 m0, s56
	s_nop 0
	buffer_load_dwordx4 v210, s[4:7], s71 offen lds
	s_mov_b32 m0, s57
	s_nop 0
	buffer_load_dwordx4 v211, s[4:7], s71 offen lds
	s_mov_b32 m0, s54
	s_nop 0
	buffer_load_dwordx4 v136, s[4:7], s70 offen lds
	s_mov_b32 m0, s55
	s_nop 0
	buffer_load_dwordx4 v137, s[4:7], s70 offen lds
	s_waitcnt vmcnt(8)
	s_waitcnt lgkmcnt(0)
	s_barrier
	s_setprio 1
	s_waitcnt lgkmcnt(7)
	v_mfma_i32_16x16x64_i8 v[60:63], v[128:131], v[178:181], v[60:63]
	v_mfma_i32_16x16x64_i8 v[56:59], v[154:157], v[178:181], v[56:59]
	s_waitcnt lgkmcnt(6)
	v_mfma_i32_16x16x64_i8 v[44:47], v[128:131], v[182:185], v[44:47]
	v_mfma_i32_16x16x64_i8 v[40:43], v[154:157], v[182:185], v[40:43]
	s_waitcnt lgkmcnt(3)
	v_mfma_i32_16x16x64_i8 v[28:31], v[128:131], v[194:197], v[28:31]
	v_mfma_i32_16x16x64_i8 v[24:27], v[154:157], v[194:197], v[24:27]
	s_waitcnt lgkmcnt(2)
	v_mfma_i32_16x16x64_i8 v[12:15], v[128:131], v[198:201], v[12:15]
	v_mfma_i32_16x16x64_i8 v[8:11], v[154:157], v[198:201], v[8:11]
	v_mfma_i32_16x16x64_i8 v[60:63], v[132:135], v[186:189], v[60:63]
	v_mfma_i32_16x16x64_i8 v[56:59], v[158:161], v[186:189], v[56:59]
	v_mfma_i32_16x16x64_i8 v[44:47], v[132:135], v[190:193], v[44:47]
	v_mfma_i32_16x16x64_i8 v[40:43], v[158:161], v[190:193], v[40:43]
	s_waitcnt lgkmcnt(1)
	v_mfma_i32_16x16x64_i8 v[28:31], v[132:135], v[202:205], v[28:31]
	v_mfma_i32_16x16x64_i8 v[24:27], v[158:161], v[202:205], v[24:27]
	s_waitcnt lgkmcnt(0)
	v_mfma_i32_16x16x64_i8 v[12:15], v[132:135], v[206:209], v[12:15]
	v_mfma_i32_16x16x64_i8 v[8:11], v[158:161], v[206:209], v[8:11]
	s_setprio 0
	s_setprio 1
	v_mfma_i32_16x16x64_i8 v[52:55], v[162:165], v[178:181], v[52:55]
	v_mfma_i32_16x16x64_i8 v[48:51], v[170:173], v[178:181], v[48:51]
	v_mfma_i32_16x16x64_i8 v[36:39], v[162:165], v[182:185], v[36:39]
	v_mfma_i32_16x16x64_i8 v[32:35], v[170:173], v[182:185], v[32:35]
	v_mfma_i32_16x16x64_i8 v[20:23], v[162:165], v[194:197], v[20:23]
	v_mfma_i32_16x16x64_i8 v[16:19], v[170:173], v[194:197], v[16:19]
	v_mfma_i32_16x16x64_i8 v[4:7], v[162:165], v[198:201], v[4:7]
	v_mfma_i32_16x16x64_i8 v[0:3], v[170:173], v[198:201], v[0:3]
	v_mfma_i32_16x16x64_i8 v[52:55], v[166:169], v[186:189], v[52:55]
	v_mfma_i32_16x16x64_i8 v[48:51], v[174:177], v[186:189], v[48:51]
	v_mfma_i32_16x16x64_i8 v[36:39], v[166:169], v[190:193], v[36:39]
	v_mfma_i32_16x16x64_i8 v[32:35], v[174:177], v[190:193], v[32:35]
	v_mfma_i32_16x16x64_i8 v[20:23], v[166:169], v[202:205], v[20:23]
	v_mfma_i32_16x16x64_i8 v[16:19], v[174:177], v[202:205], v[16:19]
	v_mfma_i32_16x16x64_i8 v[4:7], v[166:169], v[206:209], v[4:7]
	v_mfma_i32_16x16x64_i8 v[0:3], v[174:177], v[206:209], v[0:3]
	s_setprio 0
	s_barrier
	s_add_i32 s69, s69, 2
	s_addk_i32 s2, 0x100
	s_addk_i32 s3, 0x100
	s_cmp_gt_u32 s69, 13
	s_cbranch_scc0 .LBB0_959
	s_and_b64 vcc, exec, s[18:19]
	s_cbranch_vccz .LBB0_962
	s_barrier
; DI unsigned pk2(float a, float b) { f32x2 f = {a, b}; bf16x2_t h = __builtin_convertvector(f, bf16x2_t); return __builtin_bit_cast(unsigned, h); }
;     __device__ __forceinline__ void operator()(const f32x4 (&acc)[2][2][4][2], const Unit& u, int wr, int wc, int fr, int fq) const {
;         const int row0 = u.a0 * BM + wr * 64 + fr, col0 = u.a1 * BM + wc * 32 + 4 * fq;
;         const int b = (u.a0 * BM) / SEQ; const float* gt = modf + (size_t)b * NMOD + 2 * D;
;         f32x4 gv[2][2];
; #pragma unroll
;         for (int bj = 0; bj < 2; ++bj)
; #pragma unroll
;             for (int n = 0; n < 2; ++n) gv[bj][n] = *(const f32x4*)(gt + col0 + bj * HALF + n * 16) * *(const f32x4*)(wosc + col0 + bj * HALF + n * 16);
; #pragma unroll
;         for (int ai = 0; ai < 2; ++ai)
; #pragma unroll
;             for (int m = 0; m < 4; ++m) { const int row = row0 + ai * HALF + m * 16; const float sr = asc[row]; const size_t off = (size_t)row * D + col0;
; #pragma unroll
;                 for (int bj = 0; bj < 2; ++bj)
; #pragma unroll
;                     for (int n = 0; n < 2; ++n) { const f32x4 xv = *(const f32x4*)(x + off + bj * HALF + n * 16); const f32x4 r = xv + gv[bj][n] * (__builtin_convertvector(__builtin_bit_cast(i32x4_t, acc[ai][bj][m][n]), f32x4) * sr);
;                         u32x2 w; w.x = pk2(r[0], r[1]); w.y = pk2(r[2], r[3]); *(u32x2*)(x1 + off + bj * HALF + n * 16) = w; } }
.LBB0_962:
	v_mbcnt_lo_u32_b32 v130, -1, 0
	v_mbcnt_hi_u32_b32 v130, -1, v130
	s_lshl_b32 s2, s67, 8
	s_add_i32 s4, s2, s59
	s_lshl_b32 s2, s68, 8
	v_ashrrev_i32_e32 v128, 1, v130
	s_or_b32 s2, s2, s60
	v_and_b32_e32 v128, -8, v128
	v_add_u32_e32 v132, s2, v128
	s_ashr_i32 s2, s67, 31
	s_lshr_b32 s2, s2, 26
	s_add_i32 s2, s67, s2
	s_ashr_i32 s2, s2, 6
	v_readlane_b32 s68, v254, 2
	s_mul_hi_i32 s3, s2, 0xc000
	s_mul_i32 s2, s2, 0xc000
	v_readlane_b32 s70, v254, 4
	v_readlane_b32 s71, v254, 5
	s_add_u32 s2, s70, s2
	v_ashrrev_i32_e32 v133, 31, v132
	s_addc_u32 s3, s71, s3
	v_lshlrev_b64 v[128:129], 2, v[132:133]
	v_lshl_add_u64 v[166:167], s[2:3], 0, v[128:129]
	v_and_or_b32 v134, v130, 15, s4
	v_lshl_add_u64 v[186:187], s[16:17], 0, v[128:129]
	v_add_co_u32_e32 v128, vcc, s62, v166
	v_ashrrev_i32_e32 v135, 31, v134
	s_nop 0
	v_addc_co_u32_e32 v129, vcc, 0, v167, vcc
	v_lshlrev_b64 v[130:131], 11, v[134:135]
	global_load_dwordx4 v[154:157], v[128:129], off
	global_load_dwordx4 v[158:161], v[186:187], off
	v_lshl_add_u64 v[128:129], v[134:135], 2, s[14:15]
	v_lshl_add_u64 v[130:131], v[130:131], 0, v[132:133]
	global_load_dword v190, v[128:129], off
	v_lshl_add_u64 v[192:193], v[130:131], 2, s[36:37]
	global_load_dwordx4 v[162:165], v[192:193], off
	global_load_dwordx4 v[216:219], v[192:193], off offset:16
	global_load_dwordx4 v[220:223], v[192:193], off offset:512
	global_load_dwordx4 v[224:227], v[192:193], off offset:528
	global_load_dword v248, v[128:129], off offset:64
	v_or_b32_e32 v246, 16, v134
	v_ashrrev_i32_e32 v247, 31, v246
	v_lshlrev_b64 v[246:247], 11, v[246:247]
	v_lshl_add_u64 v[246:247], v[246:247], 0, v[132:133]
	v_lshl_add_u64 v[244:245], v[246:247], 2, s[36:37]
	global_load_dwordx4 v[228:231], v[244:245], off
	global_load_dwordx4 v[232:235], v[244:245], off offset:16
	global_load_dwordx4 v[236:239], v[244:245], off offset:512
	global_load_dwordx4 v[240:243], v[244:245], off offset:528
	v_cvt_f32_i32_e32 v127, v127
	v_cvt_f32_i32_e32 v126, v126
	v_cvt_f32_i32_e32 v125, v125
	v_cvt_f32_i32_e32 v124, v124
	v_lshl_add_u64 v[194:195], v[130:131], 1, s[12:13]
	v_lshl_add_u64 v[182:183], v[166:167], 0, s[20:21]
	global_load_dwordx4 v[166:169], v[186:187], off offset:16
	global_load_dwordx4 v[170:173], v[186:187], off offset:512
	global_load_dwordx4 v[174:177], v[182:183], off offset:16
	global_load_dwordx4 v[178:181], v[182:183], off offset:512
	s_nop 0
	global_load_dwordx4 v[182:185], v[182:183], off offset:528
	s_nop 0
	global_load_dwordx4 v[186:189], v[186:187], off offset:528
	v_cvt_f32_i32_e32 v123, v123
	v_cvt_f32_i32_e32 v121, v121
	v_cvt_f32_i32_e32 v120, v120
	v_cvt_f32_i32_e32 v122, v122
	v_cvt_f32_i32_e32 v119, v119
	v_cvt_f32_i32_e32 v117, v117
	v_cvt_f32_i32_e32 v116, v116
	v_cvt_f32_i32_e32 v118, v118
	v_cvt_f32_i32_e32 v115, v115
	v_cvt_f32_i32_e32 v114, v114
	v_cvt_f32_i32_e32 v113, v113
	v_cvt_f32_i32_e32 v112, v112
	v_cvt_f32_i32_e32 v111, v111
	v_cvt_f32_i32_e32 v109, v109
	v_cvt_f32_i32_e32 v108, v108
	v_cvt_f32_i32_e32 v110, v110
	v_cvt_f32_i32_e32 v107, v107
	v_cvt_f32_i32_e32 v105, v105
	v_cvt_f32_i32_e32 v104, v104
	v_cvt_f32_i32_e32 v106, v106
	v_cvt_f32_i32_e32 v103, v103
	v_cvt_f32_i32_e32 v101, v101
	v_cvt_f32_i32_e32 v100, v100
	v_cvt_f32_i32_e32 v102, v102
	v_cvt_f32_i32_e32 v99, v99
	v_cvt_f32_i32_e32 v98, v98
	v_cvt_f32_i32_e32 v97, v97
	v_cvt_f32_i32_e32 v96, v96
	v_cvt_f32_i32_e32 v95, v95
	v_cvt_f32_i32_e32 v93, v93
	v_cvt_f32_i32_e32 v92, v92
	v_cvt_f32_i32_e32 v94, v94
	v_cvt_f32_i32_e32 v91, v91
	v_cvt_f32_i32_e32 v89, v89
	v_cvt_f32_i32_e32 v88, v88
	v_cvt_f32_i32_e32 v90, v90
	v_cvt_f32_i32_e32 v87, v87
	v_cvt_f32_i32_e32 v85, v85
	v_cvt_f32_i32_e32 v84, v84
	v_cvt_f32_i32_e32 v86, v86
	v_cvt_f32_i32_e32 v83, v83
	v_cvt_f32_i32_e32 v82, v82
	v_cvt_f32_i32_e32 v81, v81
	v_cvt_f32_i32_e32 v80, v80
	v_cvt_f32_i32_e32 v79, v79
	v_cvt_f32_i32_e32 v77, v77
	v_cvt_f32_i32_e32 v76, v76
	v_cvt_f32_i32_e32 v78, v78
	v_cvt_f32_i32_e32 v75, v75
	v_cvt_f32_i32_e32 v73, v73
	v_cvt_f32_i32_e32 v72, v72
	v_cvt_f32_i32_e32 v74, v74
	v_cvt_f32_i32_e32 v71, v71
	v_cvt_f32_i32_e32 v69, v69
	v_cvt_f32_i32_e32 v68, v68
	v_cvt_f32_i32_e32 v70, v70
	v_cvt_f32_i32_e32 v67, v67
	v_cvt_f32_i32_e32 v65, v65
	v_cvt_f32_i32_e32 v64, v64
	v_cvt_f32_i32_e32 v66, v66
	v_cvt_f32_i32_e32 v63, v63
	v_cvt_f32_i32_e32 v61, v61
	v_cvt_f32_i32_e32 v60, v60
	v_cvt_f32_i32_e32 v62, v62
	v_cvt_f32_i32_e32 v59, v59
	v_cvt_f32_i32_e32 v57, v57
	v_cvt_f32_i32_e32 v56, v56
	v_cvt_f32_i32_e32 v58, v58
	v_cvt_f32_i32_e32 v55, v55
	v_cvt_f32_i32_e32 v53, v53
	s_waitcnt vmcnt(15)
	v_pk_mul_f32 v[196:197], v[190:191], v[124:125] op_sel_hi:[0,1]
	v_pk_mul_f32 v[198:199], v[190:191], v[126:127] op_sel_hi:[0,1]
	v_pk_mul_f32 v[124:125], v[156:157], v[160:161]
	v_pk_mul_f32 v[126:127], v[154:155], v[158:159]
	s_waitcnt vmcnt(14)
	v_pk_fma_f32 v[154:155], v[124:125], v[198:199], v[164:165]
	v_pk_fma_f32 v[156:157], v[126:127], v[196:197], v[162:163]
	v_pk_mul_f32 v[158:159], v[190:191], v[120:121] op_sel_hi:[0,1]
	v_cvt_pk_bf16_f32 v200, v156, v157
	v_cvt_pk_bf16_f32 v201, v154, v155
	v_pk_mul_f32 v[160:161], v[190:191], v[122:123] op_sel_hi:[0,1]
	s_waitcnt vmcnt(3)
	v_pk_mul_f32 v[120:121], v[176:177], v[168:169]
	v_pk_mul_f32 v[122:123], v[174:175], v[166:167]
	v_pk_mul_f32 v[162:163], v[190:191], v[112:113] op_sel_hi:[0,1]
	v_pk_mul_f32 v[164:165], v[190:191], v[114:115] op_sel_hi:[0,1]
	s_waitcnt vmcnt(0)
; DI unsigned pk2(float a, float b) { f32x2 f = {a, b}; bf16x2_t h = __builtin_convertvector(f, bf16x2_t); return __builtin_bit_cast(unsigned, h); }
;     __device__ __forceinline__ void operator()(const f32x4 (&acc)[2][2][4][2], const Unit& u, int wr, int wc, int fr, int fq) const {
;     ...
;         for (int ai = 0; ai < 2; ++ai)
; #pragma unroll
;             for (int m = 0; m < 4; ++m) { const int row = row0 + ai * HALF + m * 16; const float sr = asc[row]; const size_t off = (size_t)row * D + col0;
; #pragma unroll
;                 for (int bj = 0; bj < 2; ++bj)
; #pragma unroll
;                     for (int n = 0; n < 2; ++n) { const f32x4 xv = *(const f32x4*)(x + off + bj * HALF + n * 16); const f32x4 r = xv + gv[bj][n] * (__builtin_convertvector(__builtin_bit_cast(i32x4_t, acc[ai][bj][m][n]), f32x4) * sr);
;                         u32x2 w; w.x = pk2(r[0], r[1]); w.y = pk2(r[2], r[3]); *(u32x2*)(x1 + off + bj * HALF + n * 16) = w; } }
	v_pk_mul_f32 v[112:113], v[184:185], v[188:189]
	v_pk_mul_f32 v[114:115], v[182:183], v[186:187]
	v_cvt_f32_i32_e32 v52, v52
	v_cvt_f32_i32_e32 v54, v54
	v_cvt_f32_i32_e32 v51, v51
	v_cvt_f32_i32_e32 v49, v49
	v_cvt_f32_i32_e32 v48, v48
	v_cvt_f32_i32_e32 v50, v50
	v_cvt_f32_i32_e32 v47, v47
	v_cvt_f32_i32_e32 v45, v45
	v_cvt_f32_i32_e32 v44, v44
	v_cvt_f32_i32_e32 v46, v46
	v_cvt_f32_i32_e32 v43, v43
	v_cvt_f32_i32_e32 v41, v41
	v_cvt_f32_i32_e32 v40, v40
	v_cvt_f32_i32_e32 v42, v42
	v_cvt_f32_i32_e32 v39, v39
	v_cvt_f32_i32_e32 v37, v37
	v_cvt_f32_i32_e32 v36, v36
	v_cvt_f32_i32_e32 v38, v38
	v_cvt_f32_i32_e32 v35, v35
	v_cvt_f32_i32_e32 v33, v33
	v_cvt_f32_i32_e32 v32, v32
	v_cvt_f32_i32_e32 v34, v34
	v_cvt_f32_i32_e32 v31, v31
	v_cvt_f32_i32_e32 v29, v29
	v_cvt_f32_i32_e32 v28, v28
	v_cvt_f32_i32_e32 v30, v30
	v_cvt_f32_i32_e32 v27, v27
	v_cvt_f32_i32_e32 v25, v25
	v_cvt_f32_i32_e32 v24, v24
	v_cvt_f32_i32_e32 v26, v26
	v_cvt_f32_i32_e32 v23, v23
	v_cvt_f32_i32_e32 v21, v21
	v_cvt_f32_i32_e32 v20, v20
	v_cvt_f32_i32_e32 v22, v22
	v_cvt_f32_i32_e32 v19, v19
	v_cvt_f32_i32_e32 v17, v17
	v_cvt_f32_i32_e32 v16, v16
	v_cvt_f32_i32_e32 v18, v18
	v_cvt_f32_i32_e32 v15, v15
	v_cvt_f32_i32_e32 v13, v13
	v_cvt_f32_i32_e32 v12, v12
	v_cvt_f32_i32_e32 v14, v14
	v_cvt_f32_i32_e32 v11, v11
	v_cvt_f32_i32_e32 v9, v9
	v_cvt_f32_i32_e32 v8, v8
	v_cvt_f32_i32_e32 v10, v10
	v_cvt_f32_i32_e32 v7, v7
	v_cvt_f32_i32_e32 v5, v5
	v_cvt_f32_i32_e32 v4, v4
	v_cvt_f32_i32_e32 v6, v6
	v_cvt_f32_i32_e32 v3, v3
	v_cvt_f32_i32_e32 v2, v2
	v_cvt_f32_i32_e32 v1, v1
	v_cvt_f32_i32_e32 v0, v0
	s_andn2_b64 vcc, exec, s[44:45]
	s_mov_b64 s[2:3], -1
	v_readlane_b32 s69, v254, 3
	v_pk_fma_f32 v[156:157], v[120:121], v[160:161], v[218:219]
	v_pk_fma_f32 v[154:155], v[122:123], v[158:159], v[216:217]
	v_pk_mul_f32 v[158:159], v[190:191], v[116:117] op_sel_hi:[0,1]
	v_cvt_pk_bf16_f32 v202, v154, v155
	v_cvt_pk_bf16_f32 v203, v156, v157
	global_store_dwordx4 v[194:195], v[200:203], off
	v_pk_mul_f32 v[160:161], v[190:191], v[118:119] op_sel_hi:[0,1]
	v_pk_mul_f32 v[116:117], v[180:181], v[172:173]
	v_pk_mul_f32 v[118:119], v[178:179], v[170:171]
	v_pk_fma_f32 v[156:157], v[116:117], v[160:161], v[222:223]
	v_pk_fma_f32 v[154:155], v[118:119], v[158:159], v[220:221]
	v_or_b32_e32 v158, 16, v134
	v_cvt_pk_bf16_f32 v204, v154, v155
	v_cvt_pk_bf16_f32 v205, v156, v157
	v_ashrrev_i32_e32 v159, 31, v158
	v_lshl_add_u64 v[160:161], v[158:159], 2, s[14:15]
	v_lshlrev_b64 v[158:159], 11, v[158:159]
	v_lshl_add_u64 v[158:159], v[158:159], 0, v[132:133]
	v_pk_fma_f32 v[156:157], v[112:113], v[164:165], v[226:227]
	v_pk_fma_f32 v[154:155], v[114:115], v[162:163], v[224:225]
	v_lshl_add_u64 v[162:163], v[158:159], 2, s[36:37]
	v_cvt_pk_bf16_f32 v206, v154, v155
	v_cvt_pk_bf16_f32 v207, v156, v157
	global_store_dwordx4 v[194:195], v[204:207], off offset:256
	v_lshl_add_u64 v[158:159], v[158:159], 1, s[12:13]
	global_load_dword v250, v[128:129], off offset:128
	v_or_b32_e32 v246, 32, v134
	v_ashrrev_i32_e32 v247, 31, v246
	v_lshlrev_b64 v[246:247], 11, v[246:247]
	v_lshl_add_u64 v[246:247], v[246:247], 0, v[132:133]
	v_lshl_add_u64 v[244:245], v[246:247], 2, s[36:37]
	global_load_dwordx4 v[212:215], v[244:245], off
	global_load_dwordx4 v[216:219], v[244:245], off offset:16
	global_load_dwordx4 v[220:223], v[244:245], off offset:512
	global_load_dwordx4 v[224:227], v[244:245], off offset:528
	v_pk_mul_f32 v[108:109], v[248:249], v[108:109] op_sel_hi:[0,1]
	v_pk_mul_f32 v[110:111], v[248:249], v[110:111] op_sel_hi:[0,1]
	v_pk_fma_f32 v[110:111], v[124:125], v[110:111], v[230:231]
	v_pk_fma_f32 v[108:109], v[126:127], v[108:109], v[228:229]
	v_pk_mul_f32 v[104:105], v[248:249], v[104:105] op_sel_hi:[0,1]
	v_cvt_pk_bf16_f32 v200, v108, v109
	v_cvt_pk_bf16_f32 v201, v110, v111
	v_pk_mul_f32 v[106:107], v[248:249], v[106:107] op_sel_hi:[0,1]
	v_pk_mul_f32 v[100:101], v[248:249], v[100:101] op_sel_hi:[0,1]
	v_pk_mul_f32 v[102:103], v[248:249], v[102:103] op_sel_hi:[0,1]
	v_pk_mul_f32 v[96:97], v[248:249], v[96:97] op_sel_hi:[0,1]
	v_pk_mul_f32 v[98:99], v[248:249], v[98:99] op_sel_hi:[0,1]
	v_pk_fma_f32 v[106:107], v[120:121], v[106:107], v[234:235]
	v_pk_fma_f32 v[104:105], v[122:123], v[104:105], v[232:233]
	s_nop 0
	v_cvt_pk_bf16_f32 v202, v104, v105
	v_cvt_pk_bf16_f32 v203, v106, v107
	global_store_dwordx4 v[158:159], v[200:203], off
	v_pk_fma_f32 v[102:103], v[116:117], v[102:103], v[238:239]
	v_pk_fma_f32 v[100:101], v[118:119], v[100:101], v[236:237]
	v_or_b32_e32 v104, 32, v134
	v_cvt_pk_bf16_f32 v204, v100, v101
	v_cvt_pk_bf16_f32 v205, v102, v103
	v_ashrrev_i32_e32 v105, 31, v104
	v_lshl_add_u64 v[106:107], v[104:105], 2, s[14:15]
	v_lshlrev_b64 v[104:105], 11, v[104:105]
	v_lshl_add_u64 v[104:105], v[104:105], 0, v[132:133]
	v_pk_fma_f32 v[98:99], v[112:113], v[98:99], v[242:243]
	v_pk_fma_f32 v[96:97], v[114:115], v[96:97], v[240:241]
	v_lshl_add_u64 v[102:103], v[104:105], 2, s[36:37]
	v_cvt_pk_bf16_f32 v206, v96, v97
	v_cvt_pk_bf16_f32 v207, v98, v99
	global_store_dwordx4 v[158:159], v[204:207], off offset:256
	v_lshl_add_u64 v[104:105], v[104:105], 1, s[12:13]
	global_load_dword v248, v[128:129], off offset:192
	v_or_b32_e32 v246, 48, v134
	v_ashrrev_i32_e32 v247, 31, v246
	v_lshlrev_b64 v[246:247], 11, v[246:247]
	v_lshl_add_u64 v[246:247], v[246:247], 0, v[132:133]
	v_lshl_add_u64 v[244:245], v[246:247], 2, s[36:37]
	global_load_dwordx4 v[228:231], v[244:245], off
	global_load_dwordx4 v[232:235], v[244:245], off offset:16
	global_load_dwordx4 v[236:239], v[244:245], off offset:512
	global_load_dwordx4 v[240:243], v[244:245], off offset:528
	s_waitcnt vmcnt(11)
; DI unsigned pk2(float a, float b) { f32x2 f = {a, b}; bf16x2_t h = __builtin_convertvector(f, bf16x2_t); return __builtin_bit_cast(unsigned, h); }
;     __device__ __forceinline__ void operator()(const f32x4 (&acc)[2][2][4][2], const Unit& u, int wr, int wc, int fr, int fq) const {
;     ...
;         for (int ai = 0; ai < 2; ++ai)
; #pragma unroll
;             for (int m = 0; m < 4; ++m) { const int row = row0 + ai * HALF + m * 16; const float sr = asc[row]; const size_t off = (size_t)row * D + col0;
; #pragma unroll
;                 for (int bj = 0; bj < 2; ++bj)
; #pragma unroll
;                     for (int n = 0; n < 2; ++n) { const f32x4 xv = *(const f32x4*)(x + off + bj * HALF + n * 16); const f32x4 r = xv + gv[bj][n] * (__builtin_convertvector(__builtin_bit_cast(i32x4_t, acc[ai][bj][m][n]), f32x4) * sr);
;                         u32x2 w; w.x = pk2(r[0], r[1]); w.y = pk2(r[2], r[3]); *(u32x2*)(x1 + off + bj * HALF + n * 16) = w; } }
	v_pk_mul_f32 v[92:93], v[250:251], v[92:93] op_sel_hi:[0,1]
	v_pk_mul_f32 v[94:95], v[250:251], v[94:95] op_sel_hi:[0,1]
	s_waitcnt vmcnt(10)
	v_pk_fma_f32 v[94:95], v[124:125], v[94:95], v[214:215]
	v_pk_fma_f32 v[92:93], v[126:127], v[92:93], v[212:213]
	v_pk_mul_f32 v[88:89], v[250:251], v[88:89] op_sel_hi:[0,1]
	v_cvt_pk_bf16_f32 v200, v92, v93
	v_cvt_pk_bf16_f32 v201, v94, v95
	v_pk_mul_f32 v[90:91], v[250:251], v[90:91] op_sel_hi:[0,1]
	v_pk_mul_f32 v[84:85], v[250:251], v[84:85] op_sel_hi:[0,1]
	v_pk_mul_f32 v[86:87], v[250:251], v[86:87] op_sel_hi:[0,1]
	v_pk_mul_f32 v[80:81], v[250:251], v[80:81] op_sel_hi:[0,1]
	v_pk_mul_f32 v[82:83], v[250:251], v[82:83] op_sel_hi:[0,1]
	s_waitcnt vmcnt(9)
	v_pk_fma_f32 v[90:91], v[120:121], v[90:91], v[218:219]
	v_pk_fma_f32 v[88:89], v[122:123], v[88:89], v[216:217]
	s_nop 0
	v_cvt_pk_bf16_f32 v202, v88, v89
	v_cvt_pk_bf16_f32 v203, v90, v91
	global_store_dwordx4 v[104:105], v[200:203], off
	s_waitcnt vmcnt(9)
	v_pk_fma_f32 v[86:87], v[116:117], v[86:87], v[222:223]
	v_pk_fma_f32 v[84:85], v[118:119], v[84:85], v[220:221]
	v_or_b32_e32 v88, 48, v134
	v_cvt_pk_bf16_f32 v204, v84, v85
	v_cvt_pk_bf16_f32 v205, v86, v87
	v_ashrrev_i32_e32 v89, 31, v88
	v_lshl_add_u64 v[90:91], v[88:89], 2, s[14:15]
	v_lshlrev_b64 v[88:89], 11, v[88:89]
	v_lshl_add_u64 v[88:89], v[88:89], 0, v[132:133]
	s_waitcnt vmcnt(8)
	v_pk_fma_f32 v[82:83], v[112:113], v[82:83], v[226:227]
	v_pk_fma_f32 v[80:81], v[114:115], v[80:81], v[224:225]
	v_lshl_add_u64 v[86:87], v[88:89], 2, s[36:37]
	v_cvt_pk_bf16_f32 v206, v80, v81
	v_cvt_pk_bf16_f32 v207, v82, v83
	global_store_dwordx4 v[104:105], v[204:207], off offset:256
	v_lshl_add_u64 v[88:89], v[88:89], 1, s[12:13]
	global_load_dword v250, v[128:129], off offset:512
	v_lshl_add_u64 v[246:247], v[130:131], 0, s[22:23]
	v_lshl_add_u64 v[244:245], v[246:247], 2, s[36:37]
	global_load_dwordx4 v[212:215], v[244:245], off
	global_load_dwordx4 v[216:219], v[244:245], off offset:16
	global_load_dwordx4 v[220:223], v[244:245], off offset:512
	global_load_dwordx4 v[224:227], v[244:245], off offset:528
	s_waitcnt vmcnt(11)
	v_pk_mul_f32 v[76:77], v[248:249], v[76:77] op_sel_hi:[0,1]
	v_pk_mul_f32 v[78:79], v[248:249], v[78:79] op_sel_hi:[0,1]
	s_waitcnt vmcnt(10)
	v_pk_fma_f32 v[78:79], v[124:125], v[78:79], v[230:231]
	v_pk_fma_f32 v[76:77], v[126:127], v[76:77], v[228:229]
	v_pk_mul_f32 v[72:73], v[248:249], v[72:73] op_sel_hi:[0,1]
	v_cvt_pk_bf16_f32 v200, v76, v77
	v_cvt_pk_bf16_f32 v201, v78, v79
	v_pk_mul_f32 v[74:75], v[248:249], v[74:75] op_sel_hi:[0,1]
	v_pk_mul_f32 v[68:69], v[248:249], v[68:69] op_sel_hi:[0,1]
	v_pk_mul_f32 v[70:71], v[248:249], v[70:71] op_sel_hi:[0,1]
	v_pk_mul_f32 v[64:65], v[248:249], v[64:65] op_sel_hi:[0,1]
	v_pk_mul_f32 v[66:67], v[248:249], v[66:67] op_sel_hi:[0,1]
	s_waitcnt vmcnt(9)
	v_pk_fma_f32 v[74:75], v[120:121], v[74:75], v[234:235]
	v_pk_fma_f32 v[72:73], v[122:123], v[72:73], v[232:233]
	s_nop 0
	v_cvt_pk_bf16_f32 v202, v72, v73
	v_cvt_pk_bf16_f32 v203, v74, v75
	global_store_dwordx4 v[88:89], v[200:203], off
	s_waitcnt vmcnt(9)
	v_pk_fma_f32 v[70:71], v[116:117], v[70:71], v[238:239]
	v_pk_fma_f32 v[68:69], v[118:119], v[68:69], v[236:237]
	v_lshl_add_u64 v[72:73], v[130:131], 0, s[22:23]
	v_cvt_pk_bf16_f32 v204, v68, v69
	v_cvt_pk_bf16_f32 v205, v70, v71
	s_waitcnt vmcnt(8)
	v_pk_fma_f32 v[66:67], v[112:113], v[66:67], v[242:243]
	v_pk_fma_f32 v[64:65], v[114:115], v[64:65], v[240:241]
	v_lshl_add_u64 v[70:71], v[72:73], 2, s[36:37]
	v_cvt_pk_bf16_f32 v206, v64, v65
	v_cvt_pk_bf16_f32 v207, v66, v67
	global_store_dwordx4 v[88:89], v[204:207], off offset:256
	v_lshl_add_u64 v[72:73], v[72:73], 1, s[12:13]
	global_load_dword v248, v[128:129], off offset:576
	v_lshl_add_u64 v[246:247], v[130:131], 0, s[38:39]
	v_lshl_add_u64 v[244:245], v[246:247], 2, s[36:37]
	global_load_dwordx4 v[228:231], v[244:245], off
	global_load_dwordx4 v[232:235], v[244:245], off offset:16
	global_load_dwordx4 v[236:239], v[244:245], off offset:512
	global_load_dwordx4 v[240:243], v[244:245], off offset:528
	s_waitcnt vmcnt(11)
	v_pk_mul_f32 v[60:61], v[250:251], v[60:61] op_sel_hi:[0,1]
	v_pk_mul_f32 v[62:63], v[250:251], v[62:63] op_sel_hi:[0,1]
	s_waitcnt vmcnt(10)
	v_pk_fma_f32 v[62:63], v[124:125], v[62:63], v[214:215]
	v_pk_fma_f32 v[60:61], v[126:127], v[60:61], v[212:213]
	v_pk_mul_f32 v[56:57], v[250:251], v[56:57] op_sel_hi:[0,1]
	v_cvt_pk_bf16_f32 v200, v60, v61
	v_cvt_pk_bf16_f32 v201, v62, v63
	v_pk_mul_f32 v[58:59], v[250:251], v[58:59] op_sel_hi:[0,1]
	v_pk_mul_f32 v[52:53], v[250:251], v[52:53] op_sel_hi:[0,1]
	v_pk_mul_f32 v[54:55], v[250:251], v[54:55] op_sel_hi:[0,1]
	v_pk_mul_f32 v[48:49], v[250:251], v[48:49] op_sel_hi:[0,1]
	v_pk_mul_f32 v[50:51], v[250:251], v[50:51] op_sel_hi:[0,1]
	s_waitcnt vmcnt(9)
	v_pk_fma_f32 v[58:59], v[120:121], v[58:59], v[218:219]
	v_pk_fma_f32 v[56:57], v[122:123], v[56:57], v[216:217]
	s_nop 0
	v_cvt_pk_bf16_f32 v202, v56, v57
	v_cvt_pk_bf16_f32 v203, v58, v59
	global_store_dwordx4 v[72:73], v[200:203], off
	s_waitcnt vmcnt(9)
	v_pk_fma_f32 v[54:55], v[116:117], v[54:55], v[222:223]
	v_pk_fma_f32 v[52:53], v[118:119], v[52:53], v[220:221]
	v_lshl_add_u64 v[56:57], v[130:131], 0, s[38:39]
	v_cvt_pk_bf16_f32 v204, v52, v53
	v_cvt_pk_bf16_f32 v205, v54, v55
	s_waitcnt vmcnt(8)
; DI int lane_id() { int l; asm volatile("v_mbcnt_lo_u32_b32 %0, -1, 0\n\tv_mbcnt_hi_u32_b32 %0, -1, %0" : "=v"(l)); return l; }
; DI unsigned pk2(float a, float b) { f32x2 f = {a, b}; bf16x2_t h = __builtin_convertvector(f, bf16x2_t); return __builtin_bit_cast(unsigned, h); }
; #define PG8_BAR __builtin_amdgcn_s_barrier()
;     ...
;         if constexpr (ALIGN_EPI) { if (wr == 0) PG8_BAR; }
;         { int l2 = lane_id(); asm volatile("" : "+v"(l2)); cur.buf = ui & 1; E(acc, cur, wr, wc, l2 & 15, l2 >> 4); }
;         if (!has_next) break;
; #pragma unroll
;         for (int a = 0; a < 2; ++a)
; #pragma unroll
;             for (int b = 0; b < 2; ++b)
; #pragma unroll
;                 for (int m = 0; m < 4; ++m)
; #pragma unroll
;                     for (int n = 0; n < 2; ++n) acc[a][b][m][n] = (f32x4){0.f, 0.f, 0.f, 0.f};
;         cur = nxt; cA = nA; cB = nB; ++ui;
;         if constexpr (ALIGN_EPI) { if (wr == 1) PG8_BAR; }
;     }
;     __device__ __forceinline__ void operator()(const f32x4 (&acc)[2][2][4][2], const Unit& u, int wr, int wc, int fr, int fq) const {
;     ...
;         for (int ai = 0; ai < 2; ++ai)
; #pragma unroll
;             for (int m = 0; m < 4; ++m) { const int row = row0 + ai * HALF + m * 16; const float sr = asc[row]; const size_t off = (size_t)row * D + col0;
; #pragma unroll
;                 for (int bj = 0; bj < 2; ++bj)
; #pragma unroll
;                     for (int n = 0; n < 2; ++n) { const f32x4 xv = *(const f32x4*)(x + off + bj * HALF + n * 16); const f32x4 r = xv + gv[bj][n] * (__builtin_convertvector(__builtin_bit_cast(i32x4_t, acc[ai][bj][m][n]), f32x4) * sr);
;                         u32x2 w; w.x = pk2(r[0], r[1]); w.y = pk2(r[2], r[3]); *(u32x2*)(x1 + off + bj * HALF + n * 16) = w; } }
	v_pk_fma_f32 v[50:51], v[112:113], v[50:51], v[226:227]
	v_pk_fma_f32 v[48:49], v[114:115], v[48:49], v[224:225]
	v_lshl_add_u64 v[54:55], v[56:57], 2, s[36:37]
	v_cvt_pk_bf16_f32 v206, v48, v49
	v_cvt_pk_bf16_f32 v207, v50, v51
	global_store_dwordx4 v[72:73], v[204:207], off offset:256
	v_lshl_add_u64 v[56:57], v[56:57], 1, s[12:13]
	global_load_dword v250, v[128:129], off offset:640
	v_lshl_add_u64 v[246:247], v[130:131], 0, s[40:41]
	v_lshl_add_u64 v[244:245], v[246:247], 2, s[36:37]
	global_load_dwordx4 v[212:215], v[244:245], off
	global_load_dwordx4 v[216:219], v[244:245], off offset:16
	global_load_dwordx4 v[220:223], v[244:245], off offset:512
	global_load_dwordx4 v[224:227], v[244:245], off offset:528
	s_waitcnt vmcnt(11)
	v_pk_mul_f32 v[44:45], v[248:249], v[44:45] op_sel_hi:[0,1]
	v_pk_mul_f32 v[46:47], v[248:249], v[46:47] op_sel_hi:[0,1]
	s_waitcnt vmcnt(10)
	v_pk_fma_f32 v[46:47], v[124:125], v[46:47], v[230:231]
	v_pk_fma_f32 v[44:45], v[126:127], v[44:45], v[228:229]
	v_pk_mul_f32 v[40:41], v[248:249], v[40:41] op_sel_hi:[0,1]
	v_cvt_pk_bf16_f32 v200, v44, v45
	v_cvt_pk_bf16_f32 v201, v46, v47
	v_pk_mul_f32 v[42:43], v[248:249], v[42:43] op_sel_hi:[0,1]
	v_pk_mul_f32 v[36:37], v[248:249], v[36:37] op_sel_hi:[0,1]
	v_pk_mul_f32 v[38:39], v[248:249], v[38:39] op_sel_hi:[0,1]
	v_pk_mul_f32 v[32:33], v[248:249], v[32:33] op_sel_hi:[0,1]
	v_pk_mul_f32 v[34:35], v[248:249], v[34:35] op_sel_hi:[0,1]
	s_waitcnt vmcnt(9)
	v_pk_fma_f32 v[42:43], v[120:121], v[42:43], v[234:235]
	v_pk_fma_f32 v[40:41], v[122:123], v[40:41], v[232:233]
	s_nop 0
	v_cvt_pk_bf16_f32 v202, v40, v41
	v_cvt_pk_bf16_f32 v203, v42, v43
	global_store_dwordx4 v[56:57], v[200:203], off
	s_waitcnt vmcnt(9)
	v_pk_fma_f32 v[38:39], v[116:117], v[38:39], v[238:239]
	v_pk_fma_f32 v[36:37], v[118:119], v[36:37], v[236:237]
	v_lshl_add_u64 v[40:41], v[130:131], 0, s[40:41]
	v_cvt_pk_bf16_f32 v204, v36, v37
	v_cvt_pk_bf16_f32 v205, v38, v39
	s_waitcnt vmcnt(8)
	v_pk_fma_f32 v[34:35], v[112:113], v[34:35], v[242:243]
	v_pk_fma_f32 v[32:33], v[114:115], v[32:33], v[240:241]
	v_lshl_add_u64 v[38:39], v[40:41], 2, s[36:37]
	v_cvt_pk_bf16_f32 v206, v32, v33
	v_cvt_pk_bf16_f32 v207, v34, v35
	global_store_dwordx4 v[56:57], v[204:207], off offset:256
	v_lshl_add_u64 v[40:41], v[40:41], 1, s[12:13]
	global_load_dword v248, v[128:129], off offset:704
	v_lshl_add_u64 v[246:247], v[130:131], 0, s[42:43]
	v_lshl_add_u64 v[244:245], v[246:247], 2, s[36:37]
	global_load_dwordx4 v[228:231], v[244:245], off
	global_load_dwordx4 v[232:235], v[244:245], off offset:16
	global_load_dwordx4 v[236:239], v[244:245], off offset:512
	global_load_dwordx4 v[240:243], v[244:245], off offset:528
	s_waitcnt vmcnt(11)
	v_pk_mul_f32 v[28:29], v[250:251], v[28:29] op_sel_hi:[0,1]
	v_pk_mul_f32 v[30:31], v[250:251], v[30:31] op_sel_hi:[0,1]
	s_waitcnt vmcnt(10)
	v_pk_fma_f32 v[30:31], v[124:125], v[30:31], v[214:215]
	v_pk_fma_f32 v[28:29], v[126:127], v[28:29], v[212:213]
	v_pk_mul_f32 v[24:25], v[250:251], v[24:25] op_sel_hi:[0,1]
	v_cvt_pk_bf16_f32 v200, v28, v29
	v_cvt_pk_bf16_f32 v201, v30, v31
	v_pk_mul_f32 v[26:27], v[250:251], v[26:27] op_sel_hi:[0,1]
	v_pk_mul_f32 v[20:21], v[250:251], v[20:21] op_sel_hi:[0,1]
	v_pk_mul_f32 v[22:23], v[250:251], v[22:23] op_sel_hi:[0,1]
	v_pk_mul_f32 v[16:17], v[250:251], v[16:17] op_sel_hi:[0,1]
	v_pk_mul_f32 v[18:19], v[250:251], v[18:19] op_sel_hi:[0,1]
	s_waitcnt vmcnt(9)
	v_pk_fma_f32 v[26:27], v[120:121], v[26:27], v[218:219]
	v_pk_fma_f32 v[24:25], v[122:123], v[24:25], v[216:217]
	s_nop 0
	v_cvt_pk_bf16_f32 v202, v24, v25
	v_cvt_pk_bf16_f32 v203, v26, v27
	global_store_dwordx4 v[40:41], v[200:203], off
	s_waitcnt vmcnt(9)
	v_pk_fma_f32 v[22:23], v[116:117], v[22:23], v[222:223]
	v_pk_fma_f32 v[20:21], v[118:119], v[20:21], v[220:221]
	v_lshl_add_u64 v[24:25], v[130:131], 0, s[42:43]
	v_cvt_pk_bf16_f32 v204, v20, v21
	v_cvt_pk_bf16_f32 v205, v22, v23
	s_waitcnt vmcnt(8)
	v_pk_fma_f32 v[18:19], v[112:113], v[18:19], v[226:227]
	v_pk_fma_f32 v[16:17], v[114:115], v[16:17], v[224:225]
	v_lshl_add_u64 v[22:23], v[24:25], 2, s[36:37]
	v_cvt_pk_bf16_f32 v206, v16, v17
	v_cvt_pk_bf16_f32 v207, v18, v19
	global_store_dwordx4 v[40:41], v[204:207], off offset:256
	v_lshl_add_u64 v[24:25], v[24:25], 1, s[12:13]
	s_waitcnt vmcnt(6)
	v_pk_mul_f32 v[12:13], v[248:249], v[12:13] op_sel_hi:[0,1]
	v_pk_mul_f32 v[14:15], v[248:249], v[14:15] op_sel_hi:[0,1]
	s_waitcnt vmcnt(5)
	v_pk_fma_f32 v[14:15], v[124:125], v[14:15], v[230:231]
	v_pk_fma_f32 v[12:13], v[126:127], v[12:13], v[228:229]
	v_pk_mul_f32 v[8:9], v[248:249], v[8:9] op_sel_hi:[0,1]
	v_cvt_pk_bf16_f32 v200, v12, v13
	v_cvt_pk_bf16_f32 v201, v14, v15
	v_pk_mul_f32 v[10:11], v[248:249], v[10:11] op_sel_hi:[0,1]
	v_pk_mul_f32 v[4:5], v[248:249], v[4:5] op_sel_hi:[0,1]
	v_pk_mul_f32 v[6:7], v[248:249], v[6:7] op_sel_hi:[0,1]
	v_pk_mul_f32 v[0:1], v[248:249], v[0:1] op_sel_hi:[0,1]
	v_pk_mul_f32 v[2:3], v[248:249], v[2:3] op_sel_hi:[0,1]
	s_waitcnt vmcnt(4)
	v_pk_fma_f32 v[10:11], v[120:121], v[10:11], v[234:235]
	v_pk_fma_f32 v[8:9], v[122:123], v[8:9], v[232:233]
	s_nop 0
	v_cvt_pk_bf16_f32 v202, v8, v9
	v_cvt_pk_bf16_f32 v203, v10, v11
	global_store_dwordx4 v[24:25], v[200:203], off
	s_waitcnt vmcnt(4)
	v_pk_fma_f32 v[6:7], v[116:117], v[6:7], v[238:239]
	v_pk_fma_f32 v[4:5], v[118:119], v[4:5], v[236:237]
	s_nop 0
	v_cvt_pk_bf16_f32 v204, v4, v5
	v_cvt_pk_bf16_f32 v205, v6, v7
	s_waitcnt vmcnt(3)
	v_pk_fma_f32 v[2:3], v[112:113], v[2:3], v[242:243]
	v_pk_fma_f32 v[0:1], v[114:115], v[0:1], v[240:241]
	s_nop 0
	v_cvt_pk_bf16_f32 v206, v0, v1
	v_cvt_pk_bf16_f32 v207, v2, v3
	global_store_dwordx4 v[24:25], v[204:207], off offset:256
	s_cbranch_vccnz .LBB0_951
	s_andn2_b64 vcc, exec, s[10:11]
	s_cbranch_vccnz .LBB0_950
	s_barrier
	s_branch .LBB0_950
